# rwkv operator images QM/PHI stored fragment-major so the chunk-serial pass loads whole contiguous KiB (on top of v35)
# speedup vs baseline: 1.0071x; 1.0037x over previous
.LBB0_380:
	v_or_b32_e32 v0, s3, v12
	v_lshl_add_u32 v13, v13, 1, v130
	v_lshl_or_b32 v30, v0, 3, s16
	v_add_u32_e32 v0, v13, v7
	s_waitcnt lgkmcnt(0)
	s_barrier
	ds_read_b64 v[20:21], v0 offset:55296
	ds_read_b128 v[0:3], v4 offset:9216
	ds_read_b128 v[22:25], v4 offset:9280
	v_add3_u32 v39, v126, v7, v44
	ds_read_b128 v[14:17], v39
	ds_read_b128 v[26:29], v39 offset:64
	s_waitcnt lgkmcnt(4)
	v_lshlrev_b32_e32 v18, 16, v20
	v_and_b32_e32 v19, 0xffff0000, v20
	v_lshlrev_b32_e32 v20, 16, v21
	v_and_b32_e32 v21, 0xffff0000, v21
	s_lshl_b32 s0, s40, 1
	s_and_b32 s1, s18, 0xffffffe0
	s_waitcnt lgkmcnt(1)
	v_mfma_f32_16x16x32_bf16 v[0:3], v[0:3], v[14:17], v[18:21]
	s_or_b32 s0, s0, s1
	s_or_b32 s0, s0, s26
	s_ashr_i32 s1, s0, 31
	s_lshl_b64 s[0:1], s[0:1], 13
	s_waitcnt lgkmcnt(0)
	v_mfma_f32_16x16x32_bf16 v[0:3], v[22:25], v[26:29], v[0:3]
	v_ashrrev_i32_e32 v31, 31, v30
	s_add_u32 s8, s17, s0
	s_addc_u32 s9, s44, s1
	v_and_b32_e32 v34, 56, v30
	v_and_b32_e32 v35, 4, v30
	v_lshlrev_b32_e32 v34, 5, v34
	v_lshl_add_u32 v34, v35, 1, v34
	v_lshl_add_u32 v34, v51, 4, v34
	v_mov_b32_e32 v35, v105
	v_lshl_add_u64 v[36:37], s[8:9], 0, v[34:35]
	v_and_b32_e32 v104, 48, v10
	v_lshlrev_b32_e32 v104, 7, v104
	s_nop 1
	v_cvt_pk_bf16_f32 v0, v0, v1
	v_cvt_pk_bf16_f32 v1, v2, v3
	v_lshl_add_u64 v[2:3], v[36:37], 0, v[104:105]
	global_store_dwordx2 v[2:3], v[0:1], off
	ds_read_b128 v[0:3], v4 offset:9216
	ds_read_b64_tr_b16 v[14:15], v11 offset:18432
	ds_read_b64_tr_b16 v[16:17], v11 offset:19008
	ds_read_b128 v[18:21], v4 offset:9280
	ds_read_b64_tr_b16 v[22:23], v11 offset:23040
	ds_read_b64_tr_b16 v[24:25], v11 offset:23616
	v_add_u32_e32 v11, v13, v5
	ds_read_b64 v[30:31], v11 offset:55296
	v_add3_u32 v40, v126, v5, v44
	s_waitcnt lgkmcnt(4)
	v_mfma_f32_16x16x32_bf16 v[14:17], v[0:3], v[14:17], 0
	ds_read_b128 v[26:29], v40
	v_lshl_add_u32 v11, v10, 2, v114
	ds_read_b32 v38, v11
	s_waitcnt lgkmcnt(3)
	v_mfma_f32_16x16x32_bf16 v[14:17], v[18:21], v[22:25], v[14:17]
	s_waitcnt lgkmcnt(2)
	v_lshlrev_b32_e32 v22, 16, v30
	v_and_b32_e32 v23, 0xffff0000, v30
	v_lshlrev_b32_e32 v24, 16, v31
	v_and_b32_e32 v25, 0xffff0000, v31
	ds_read_b128 v[30:33], v40 offset:64
	s_add_u32 s8, s45, s0
	s_waitcnt lgkmcnt(2)
	v_mfma_f32_16x16x32_bf16 v[0:3], v[0:3], v[26:29], v[22:25]
	s_addc_u32 s9, s58, s1
	v_lshl_or_b32 v26, v12, 2, s62
	v_or_b32_e32 v27, 1, v26
	s_waitcnt lgkmcnt(0)
	v_mfma_f32_16x16x32_bf16 v[0:3], v[18:21], v[30:33], v[0:3]
	v_lshl_add_u64 v[22:23], s[8:9], 0, v[34:35]
	v_lshl_add_u64 v[24:25], v[22:23], 0, v[104:105]
	v_and_b32_e32 v104, 48, v8
	v_lshlrev_b32_e32 v104, 7, v104
	v_cmp_eq_u32_e32 vcc, v26, v10
	v_or_b32_e32 v28, 3, v26
	s_nop 2
	v_cvt_pk_bf16_f32 v0, v0, v1
	v_cvt_pk_bf16_f32 v1, v2, v3
	v_lshl_add_u64 v[2:3], v[36:37], 0, v[104:105]
	global_store_dwordx2 v[2:3], v[0:1], off
	v_cndmask_b32_e64 v0, 0, 1.0, vcc
	v_cmp_eq_u32_e32 vcc, v27, v10
	v_or_b32_e32 v29, 2, v26
	v_or_b32_e32 v30, s95, v46
	v_cndmask_b32_e64 v1, 0, 1.0, vcc
	v_cmp_eq_u32_e32 vcc, v28, v10
	v_pk_add_f32 v[0:1], v[0:1], v[14:15]
	s_add_u32 s8, s59, s0
	v_cndmask_b32_e64 v3, 0, 1.0, vcc
	v_cmp_eq_u32_e32 vcc, v29, v10
	v_pk_mul_f32 v[0:1], v[38:39], v[0:1] op_sel_hi:[0,1]
	v_cvt_pk_bf16_f32 v0, v0, v1
	v_cndmask_b32_e64 v2, 0, 1.0, vcc
	v_pk_add_f32 v[2:3], v[2:3], v[16:17]
	v_cmp_eq_u32_e32 vcc, v26, v8
	v_pk_mul_f32 v[2:3], v[38:39], v[2:3] op_sel_hi:[0,1]
	v_cvt_pk_bf16_f32 v1, v2, v3
	global_store_dwordx2 v[24:25], v[0:1], off
	ds_read_b128 v[0:3], v4 offset:9216
	ds_read_b128 v[10:13], v4 offset:9280
	ds_read_b64_tr_b16 v[14:15], v9 offset:18432
	ds_read_b64_tr_b16 v[16:17], v9 offset:19008
	ds_read_b64_tr_b16 v[18:19], v9 offset:23040
	ds_read_b64_tr_b16 v[20:21], v9 offset:23616
	s_waitcnt lgkmcnt(2)
	v_mfma_f32_16x16x32_bf16 v[0:3], v[0:3], v[14:17], 0
	v_lshl_add_u32 v9, v8, 2, v114
	v_and_or_b32 v24, v47, 3, v50
	s_addc_u32 s9, s35, s1
	s_waitcnt lgkmcnt(0)
	v_mfma_f32_16x16x32_bf16 v[0:3], v[10:13], v[18:21], v[0:3]
	ds_read_b32 v10, v9
	v_cndmask_b32_e64 v12, 0, 1.0, vcc
	v_cmp_eq_u32_e32 vcc, v27, v8
	v_mul_u32_u24_e32 v20, 0x90, v24
	v_add3_u32 v26, v111, v20, v6
	v_cndmask_b32_e64 v13, 0, 1.0, vcc
	v_cmp_eq_u32_e32 vcc, v28, v8
	s_nop 0
	v_pk_add_f32 v[0:1], v[12:13], v[0:1]
	v_lshl_add_u32 v27, s62, 1, v26
	v_cndmask_b32_e64 v9, 0, 1.0, vcc
	v_cmp_eq_u32_e32 vcc, v29, v8
	s_waitcnt lgkmcnt(0)
	v_pk_mul_f32 v[0:1], v[10:11], v[0:1] op_sel_hi:[0,1]
	v_cvt_pk_bf16_f32 v0, v0, v1
	v_cndmask_b32_e64 v8, 0, 1.0, vcc
	v_pk_add_f32 v[2:3], v[8:9], v[2:3]
	v_add_u32_e32 v28, 0xfc00, v27
	v_pk_mul_f32 v[2:3], v[10:11], v[2:3] op_sel_hi:[0,1]
	v_cvt_pk_bf16_f32 v1, v2, v3
	v_lshl_add_u64 v[2:3], v[22:23], 0, v[104:105]
	global_store_dwordx2 v[2:3], v[0:1], off
	ds_read_b128 v[0:3], v4 offset:27648
	ds_read_b128 v[8:11], v39
	ds_read_b128 v[12:15], v4 offset:27712
	ds_read_b128 v[16:19], v39 offset:64
	s_waitcnt lgkmcnt(2)
	v_mfma_f32_16x16x32_bf16 v[0:3], v[0:3], v[8:11], 0
	ds_read_b64_tr_b16 v[8:9], v27 offset:64512
	ds_read_b64_tr_b16 v[10:11], v27 offset:65088
	v_add3_u32 v20, v127, v7, v44
	s_waitcnt lgkmcnt(2)
	v_mfma_f32_16x16x32_bf16 v[0:3], v[12:15], v[16:19], v[0:3]
	ds_read_b64_tr_b16 v[12:13], v28 offset:4608
	ds_read_b64_tr_b16 v[14:15], v28 offset:5184
	ds_read_b128 v[16:19], v20
	ds_read_b128 v[20:23], v20 offset:64
	v_add_u32_e32 v31, v124, v6
	v_lshl_add_u32 v32, v45, 2, v133
	s_waitcnt lgkmcnt(1)
	v_mfma_f32_16x16x32_bf16 v[0:3], v[8:11], v[16:19], v[0:3]
	v_mov_b32_e32 v8, 0x1200
	v_mad_u32_u24 v29, v24, s39, v8
	s_add_u32 s0, s56, s0
	s_waitcnt lgkmcnt(0)
	v_mfma_f32_16x16x32_bf16 v[0:3], v[12:15], v[20:23], v[0:3]
	v_add3_u32 v14, v111, v7, v44
	v_add_u32_e32 v20, s11, v26
	s_addc_u32 s1, s92, s1
	s_add_i32 s18, s18, s19
	s_cmpk_gt_i32 s18, 0x10ff
	s_nop 2
	v_cvt_pk_bf16_f32 v0, v0, v1
	v_cvt_pk_bf16_f32 v1, v2, v3
	v_or_b32_e32 v2, s93, v30
	v_ashrrev_i32_e32 v3, 31, v2
	v_lshl_add_u64 v[2:3], v[2:3], 1, s[8:9]
	global_store_dwordx2 v[2:3], v[0:1], off
	ds_read_b64_tr_b16 v[0:1], v27 offset:18432
	ds_read_b64_tr_b16 v[2:3], v27 offset:19008
	ds_read_b128 v[6:9], v14 offset:27648
	ds_read_b64_tr_b16 v[10:11], v27 offset:23040
	ds_read_b64_tr_b16 v[12:13], v27 offset:23616
	ds_read_b128 v[14:17], v14 offset:27712
	s_waitcnt lgkmcnt(3)
	v_mfma_f32_16x16x32_bf16 v[0:3], v[0:3], v[6:9], 0
	ds_read_b64_tr_b16 v[6:7], v27 offset:36864
	ds_read_b64_tr_b16 v[8:9], v27 offset:37440
	ds_read_b64_tr_b16 v[18:19], v20 offset:64512
	ds_read_b64_tr_b16 v[20:21], v20 offset:65088
	ds_read_b64_tr_b16 v[22:23], v27 offset:41472
	ds_read_b64_tr_b16 v[24:25], v27 offset:42048
	s_waitcnt lgkmcnt(6)
	v_mfma_f32_16x16x32_bf16 v[0:3], v[10:13], v[14:17], v[0:3]
	v_add3_u32 v12, v31, s11, v29
	ds_read_b64_tr_b16 v[10:11], v12
	ds_read_b64_tr_b16 v[12:13], v12 offset:576
	s_waitcnt lgkmcnt(4)
	v_mfma_f32_16x16x32_bf16 v[0:3], v[6:9], v[18:21], v[0:3]
	ds_read2_b32 v[6:7], v32 offset1:1
	ds_read2_b32 v[8:9], v32 offset0:2 offset1:3
	s_waitcnt lgkmcnt(2)
	v_mfma_f32_16x16x32_bf16 v[0:3], v[22:25], v[10:13], v[0:3]
	v_or_b32_e32 v22, s97, v46
	s_waitcnt lgkmcnt(1)
	s_nop 5
	v_pk_mul_f32 v[0:1], v[0:1], v[6:7]
	s_waitcnt lgkmcnt(0)
	v_pk_mul_f32 v[2:3], v[2:3], v[8:9]
	v_cvt_pk_bf16_f32 v0, v0, v1
	v_cvt_pk_bf16_f32 v1, v2, v3
	v_add_u32_e32 v2, s96, v22
	v_ashrrev_i32_e32 v3, 31, v2
	v_lshl_add_u64 v[2:3], v[2:3], 1, s[0:1]
	global_store_dwordx2 v[2:3], v[0:1], off
	ds_read_b128 v[0:3], v4 offset:27648
	ds_read_b128 v[6:9], v4 offset:27712
	ds_read_b128 v[10:13], v40
	ds_read_b128 v[14:17], v40 offset:64
	s_waitcnt lgkmcnt(1)
	v_mfma_f32_16x16x32_bf16 v[0:3], v[0:3], v[10:13], 0
	v_add3_u32 v4, v127, v5, v44
	s_waitcnt lgkmcnt(0)
	v_mfma_f32_16x16x32_bf16 v[0:3], v[6:9], v[14:17], v[0:3]
	ds_read_b64_tr_b16 v[6:7], v27 offset:64512
	ds_read_b64_tr_b16 v[8:9], v27 offset:65088
	ds_read_b64_tr_b16 v[10:11], v28 offset:4608
	ds_read_b64_tr_b16 v[12:13], v28 offset:5184
	ds_read_b128 v[14:17], v4
	ds_read_b128 v[18:21], v4 offset:64
	s_waitcnt lgkmcnt(1)
	v_mfma_f32_16x16x32_bf16 v[0:3], v[6:9], v[14:17], v[0:3]
	s_waitcnt lgkmcnt(0)
	v_mfma_f32_16x16x32_bf16 v[0:3], v[10:13], v[18:21], v[0:3]
	v_add3_u32 v12, v111, v5, v44
	s_nop 6
	v_cvt_pk_bf16_f32 v0, v0, v1
	v_cvt_pk_bf16_f32 v1, v2, v3
	v_or_b32_e32 v2, s50, v30
	v_ashrrev_i32_e32 v3, 31, v2
	v_lshl_add_u64 v[2:3], v[2:3], 1, s[8:9]
	global_store_dwordx2 v[2:3], v[0:1], off
	ds_read_b64_tr_b16 v[0:1], v27 offset:18432
	ds_read_b64_tr_b16 v[2:3], v27 offset:19008
	ds_read_b64_tr_b16 v[4:5], v27 offset:23040
	ds_read_b64_tr_b16 v[6:7], v27 offset:23616
	ds_read_b128 v[8:11], v12 offset:27648
	ds_read_b128 v[12:15], v12 offset:27712
	s_waitcnt lgkmcnt(1)
	v_mfma_f32_16x16x32_bf16 v[0:3], v[0:3], v[8:11], 0
	ds_read_b64_tr_b16 v[8:9], v27 offset:36864
	ds_read_b64_tr_b16 v[10:11], v27 offset:37440
	s_waitcnt lgkmcnt(2)
	v_mfma_f32_16x16x32_bf16 v[0:3], v[4:7], v[12:15], v[0:3]
	v_add_u32_e32 v6, s10, v26
	ds_read_b64_tr_b16 v[4:5], v6 offset:64512
	ds_read_b64_tr_b16 v[6:7], v6 offset:65088
	ds_read_b64_tr_b16 v[12:13], v27 offset:41472
	ds_read_b64_tr_b16 v[14:15], v27 offset:42048
	s_waitcnt lgkmcnt(2)
	v_mfma_f32_16x16x32_bf16 v[0:3], v[8:11], v[4:7], v[0:3]
	v_add3_u32 v6, v31, s10, v29
	ds_read_b64_tr_b16 v[4:5], v6
	ds_read_b64_tr_b16 v[6:7], v6 offset:576
	ds_read2_b32 v[8:9], v32 offset1:1
	ds_read2_b32 v[10:11], v32 offset0:2 offset1:3
	s_waitcnt lgkmcnt(2)
	v_mfma_f32_16x16x32_bf16 v[0:3], v[12:15], v[4:7], v[0:3]
	s_waitcnt lgkmcnt(1)
	s_nop 6
	v_pk_mul_f32 v[0:1], v[0:1], v[8:9]
	s_waitcnt lgkmcnt(0)
	v_pk_mul_f32 v[2:3], v[2:3], v[10:11]
	v_cvt_pk_bf16_f32 v0, v0, v1
	v_cvt_pk_bf16_f32 v1, v2, v3
	v_add_u32_e32 v2, s6, v22
	v_ashrrev_i32_e32 v3, 31, v2
	v_lshl_add_u64 v[2:3], v[2:3], 1, s[0:1]
	global_store_dwordx2 v[2:3], v[0:1], off
	s_barrier
	s_cbranch_scc1 .LBB0_450

.LBB0_507:
	s_andn2_b64 vcc, exec, s[0:1]
	s_cbranch_vccnz .LBB0_625
	v_readlane_b32 s4, v253, 2
	v_readlane_b32 s6, v253, 4
	v_readlane_b32 s7, v253, 5
	v_readlane_b32 s10, v253, 8
	v_readlane_b32 s11, v253, 9
	s_mov_b32 s0, s92
	v_readlane_b32 s8, v253, 6
	v_readlane_b32 s9, v253, 7
	s_mov_b64 s[6:7], s[10:11]
	s_mov_b32 s50, s88
	s_waitcnt vmcnt(0) lgkmcnt(0)
	v_mbcnt_lo_u32_b32 v0, -1, 0
	v_mbcnt_hi_u32_b32 v0, -1, v0
	s_mov_b32 s51, s85
	s_mov_b64 s[2:3], s[8:9]
	s_mov_b32 s1, s84
	v_mov_b32_e32 v1, v105
	s_cmpk_gt_i32 s50, 0xff
	v_readlane_b32 s5, v253, 3
	s_cbranch_scc1 .LBB0_570
	s_and_b32 s1, s0, -2
	s_cmp_eq_u32 s1, 2
	s_cselect_b64 s[8:9], -1, 0
	s_add_u32 s10, s6, 0x35600000
	s_addc_u32 s11, s7, 0
	s_add_u32 s12, s6, 0x35900000
	s_addc_u32 s13, s7, 0
	s_and_b32 s1, s0, 3
	s_add_u32 s58, s6, 0x44600000
	s_addc_u32 s59, s7, 0
	s_cmp_lt_u32 s0, 4
	s_cselect_b64 s[14:15], -1, 0
	s_cmp_gt_u32 s0, 3
	s_cselect_b64 s[16:17], -1, 0
	s_lshl_b32 s4, s1, 10
	s_lshl_b32 s5, s1, 8
	v_and_b32_e32 v7, 15, v0
	s_lshl_b32 s1, s1, 4
	v_ashrrev_i32_e32 v4, 1, v0
	v_or_b32_e32 v113, s1, v7
	v_bitop3_b32 v114, v7, 63, s1 bitop3:0x36
	s_lshl_b32 s1, s0, 3
	v_lshl_add_u32 v3, s0, 6, v0
	v_lshlrev_b32_e32 v6, 4, v0
	v_lshlrev_b32_e32 v2, 6, v0
	v_and_b32_e32 v4, -8, v4
	v_lshlrev_b32_e32 v112, 2, v0
	v_ashrrev_i32_e32 v0, 2, v0
	s_and_b32 s68, s1, 8
	s_lshl_b32 s1, s0, 9
	v_add_u32_e32 v110, v1, v6
	v_and_b32_e32 v2, 0x3c0, v2
	v_ashrrev_i32_e32 v5, 31, v4
	v_and_b32_e32 v76, -4, v0
	s_and_b32 s1, s1, 0x400
	s_lshl_b32 s0, s0, 10
	v_add_u32_e32 v111, 0xffffff80, v3
	v_cmp_gt_i32_e64 s[2:3], s21, v3
	v_ashrrev_i32_e32 v77, 31, v76
	v_add3_u32 v115, v1, s1, v6
	v_add_u32_e32 v116, s1, v110
	v_add_u32_e32 v117, 0xfffffe00, v3
	v_add3_u32 v118, s0, v6, v1
	s_lshl_b32 s28, s4, 1
	s_lshl_b32 s44, s5, 1
	v_mov_b32_e32 v78, v6
	v_mov_b64_e32 v[80:81], 0
	s_branch .LBB0_511

.LBB0_520:
	s_bfe_u32 s45, s50, 0x10002
	s_and_b32 s61, s50, 3
	s_bfe_i32 s40, s50, 0x10002
	s_bfe_u32 s42, s50, 0x40003
	s_ashr_i32 s41, s50, 7
	s_mul_i32 s0, s45, 0x1100000
	s_add_u32 s0, s58, s0
	s_addc_u32 s1, s59, 0
	s_lshl_b32 s53, s41, 2
	s_and_b32 s24, s40, 3
	s_add_i32 s26, s53, 0x80
	s_or_b32 s52, s24, s26
	s_lshl_b32 s24, s52, 4
	s_or_b32 s54, s24, s42
	s_ashr_i32 s55, s54, 31
	s_add_u32 s34, s6, s18
	s_addc_u32 s35, s7, s19
	s_lshl_b64 s[56:57], s[54:55], 14
	s_lshl_b32 s19, s45, 13
	s_lshl_b32 s18, s45, 12
	s_or_b32 s24, s56, s19
	s_add_u32 s62, s34, s24
	s_addc_u32 s63, s35, s57
	s_add_u32 s54, s6, s4
	s_addc_u32 s55, s7, s5
	s_add_u32 s4, s54, s24
	s_addc_u32 s5, s55, s57
	s_or_b32 s24, s45, s26
	s_add_i32 s36, s24, 1
	s_lshl_b32 s24, s36, 4
	s_or_b32 s56, s24, s42
	s_ashr_i32 s57, s56, 31
	s_lshl_b64 s[56:57], s[56:57], 14
	s_or_b32 s24, s56, s19
	s_add_u32 s64, s34, s24
	s_addc_u32 s65, s35, s57
	s_add_u32 s56, s54, s24
	s_addc_u32 s57, s55, s57
	s_sub_i32 s24, s53, s45
	s_addk_i32 s24, 0x82
	s_lshl_b32 s53, s24, 4
	s_or_b32 s66, s53, s42
	s_ashr_i32 s67, s66, 31
	s_lshl_b64 s[66:67], s[66:67], 14
	s_or_b32 s53, s66, s19
	s_add_u32 s70, s34, s53
	s_addc_u32 s71, s35, s67
	s_add_u32 s66, s54, s53
	v_lshl_add_u32 v2, s61, 10, v112
	s_addc_u32 s67, s55, s67
	v_ashrrev_i32_e32 v3, 31, v2
	s_cmp_eq_u32 s45, 0
	v_mov_b32_e32 v79, v105
	v_lshlrev_b64 v[56:57], 1, v[2:3]
	v_lshl_add_u64 v[0:1], s[62:63], 0, v[78:79]
	v_lshl_add_u64 v[2:3], s[4:5], 0, v[56:57]
	s_cselect_b64 s[4:5], -1, 0
	v_lshl_add_u64 v[0:1], v[0:1], 0, v[80:81]
	v_lshl_add_u64 v[4:5], s[56:57], 0, v[56:57]
	s_and_b64 s[56:57], s[4:5], exec
	v_lshl_add_u64 v[0:1], v[0:1], 0, s[28:29]
	s_cselect_b32 s53, 3, 0
	global_load_dwordx4 v[28:31], v[0:1], off
	global_load_dwordx4 v[24:27], v[0:1], off offset:1024
	v_lshl_add_u64 v[0:1], s[64:65], 0, v[78:79]
	s_cselect_b32 s60, 1, 62
	s_cselect_b32 s64, 2, 61
	s_or_b32 s26, s53, s26
	s_lshl_b32 s53, s26, 4
	s_or_b32 s56, s53, s42
	s_ashr_i32 s57, s56, 31
	s_lshl_b64 s[56:57], s[56:57], 14
	s_or_b32 s53, s56, s19
	s_add_u32 s62, s34, s53
	s_addc_u32 s63, s35, s57
	v_lshl_add_u64 v[10:11], s[62:63], 0, v[78:79]
	s_add_u32 s56, s54, s53
	v_lshl_add_u64 v[10:11], v[10:11], 0, v[80:81]
	s_addc_u32 s57, s55, s57
	s_and_b32 s40, s40, 63
	s_lshl_b32 s53, s41, 6
	v_lshl_add_u64 v[12:13], v[10:11], 0, s[28:29]
	v_lshl_add_u64 v[10:11], s[56:57], 0, v[56:57]
	s_or_b32 s56, s40, s53
	s_lshl_b32 s40, s56, 4
	s_mov_b32 s45, s29
	v_lshl_add_u64 v[0:1], v[0:1], 0, v[80:81]
	s_or_b32 s40, s40, s42
	v_lshl_add_u64 v[2:3], v[2:3], 0, s[44:45]
	v_lshl_add_u64 v[0:1], v[0:1], 0, s[28:29]
	s_ashr_i32 s41, s40, 31
	v_lshl_add_u64 v[4:5], v[4:5], 0, s[44:45]
	global_load_dwordx2 v[88:89], v[2:3], off
	global_load_dwordx4 v[20:23], v[0:1], off
	global_load_dwordx4 v[16:19], v[0:1], off offset:1024
	global_load_dwordx2 v[84:85], v[4:5], off
	v_lshl_add_u64 v[0:1], s[70:71], 0, v[78:79]
	s_lshl_b64 s[40:41], s[40:41], 14
	v_lshl_add_u64 v[0:1], v[0:1], 0, v[80:81]
	s_or_b32 s40, s40, s19
	v_lshl_add_u64 v[4:5], v[0:1], 0, s[28:29]
	v_lshl_add_u64 v[0:1], s[66:67], 0, v[56:57]
	s_add_u32 s62, s34, s40
	v_lshl_add_u64 v[8:9], v[0:1], 0, s[44:45]
	v_lshl_add_u64 v[32:33], v[10:11], 0, s[44:45]
	s_addc_u32 s63, s35, s41
	global_load_dwordx4 v[0:3], v[4:5], off
	s_nop 0
	global_load_dwordx4 v[4:7], v[4:5], off offset:1024
	s_nop 0
	global_load_dwordx2 v[86:87], v[8:9], off
	s_nop 0
	global_load_dwordx4 v[8:11], v[12:13], off
	s_nop 0
	global_load_dwordx4 v[12:15], v[12:13], off offset:1024
	s_nop 0
	global_load_dwordx2 v[82:83], v[32:33], off
	v_lshl_add_u64 v[32:33], s[62:63], 0, v[78:79]
	s_add_u32 s40, s54, s40
	v_lshl_add_u64 v[32:33], v[32:33], 0, v[80:81]
	s_addc_u32 s41, s55, s41
	s_or_b32 s57, s60, s53
	v_lshl_add_u64 v[36:37], v[32:33], 0, s[28:29]
	v_lshl_add_u64 v[32:33], s[40:41], 0, v[56:57]
	s_lshl_b32 s40, s57, 4
	s_or_b32 s40, s40, s42
	s_ashr_i32 s41, s40, 31
	s_lshl_b64 s[40:41], s[40:41], 14
	s_or_b32 s40, s40, s19
	s_add_u32 s62, s34, s40
	s_addc_u32 s63, s35, s41
	v_lshl_add_u64 v[42:43], s[62:63], 0, v[78:79]
	s_add_u32 s40, s54, s40
	v_lshl_add_u64 v[42:43], v[42:43], 0, v[80:81]
	s_addc_u32 s41, s55, s41
	s_or_b32 s60, s64, s53
	v_lshl_add_u64 v[44:45], v[42:43], 0, s[28:29]
	v_lshl_add_u64 v[42:43], s[40:41], 0, v[56:57]
	s_lshl_b32 s40, s60, 4
	s_or_b32 s40, s40, s42
	s_ashr_i32 s41, s40, 31
	s_lshl_b64 s[40:41], s[40:41], 14
	s_or_b32 s19, s40, s19
	s_add_u32 s62, s34, s19
	v_lshl_add_u64 v[40:41], v[32:33], 0, s[44:45]
	s_waitcnt vmcnt(14)
	v_lshl_add_u64 v[48:49], v[42:43], 0, s[44:45]
	s_addc_u32 s63, s35, s41
	global_load_dwordx4 v[32:35], v[36:37], off
	s_nop 0
	global_load_dwordx4 v[36:39], v[36:37], off offset:1024
	s_nop 0
	global_load_dwordx2 v[96:97], v[40:41], off
	s_nop 0
	global_load_dwordx4 v[40:43], v[44:45], off
	s_nop 0
	global_load_dwordx4 v[44:47], v[44:45], off offset:1024
	s_nop 0
	global_load_dwordx2 v[98:99], v[48:49], off
	v_lshl_add_u64 v[48:49], s[62:63], 0, v[78:79]
	s_add_u32 s40, s54, s19
	v_lshl_add_u64 v[48:49], v[48:49], 0, v[80:81]
	s_addc_u32 s41, s55, s41
	s_waitcnt vmcnt(19)
	v_lshl_add_u64 v[52:53], v[48:49], 0, s[28:29]
	v_lshl_add_u64 v[48:49], s[40:41], 0, v[56:57]
	v_lshl_add_u64 v[58:59], v[48:49], 0, s[44:45]
	global_load_dwordx4 v[48:51], v[52:53], off
	s_nop 0
	global_load_dwordx4 v[52:55], v[52:53], off offset:1024
	s_nop 0
	global_load_dwordx2 v[100:101], v[58:59], off
	s_lshl_b32 s41, s42, 6
	s_lshl_b32 s19, s42, 7
	s_add_u32 s19, s0, s19
	s_addc_u32 s63, s1, 0
	s_lshl_b32 s40, s61, 4
	s_lshl_b32 s61, s61, 5
	s_add_u32 s62, s19, s61
	v_lshl_add_u64 v[58:59], s[34:35], 0, v[78:79]
	s_addc_u32 s63, s63, 0
	v_lshl_add_u64 v[58:59], v[58:59], 0, v[80:81]
	v_lshl_add_u64 v[56:57], s[54:55], 0, v[56:57]
	v_cndmask_b32_e64 v104, v114, v113, s[4:5]
	v_lshl_add_u64 v[90:91], v[76:77], 1, s[62:63]
	v_lshl_add_u64 v[92:93], v[58:59], 0, s[28:29]
	v_lshl_add_u64 v[94:95], v[56:57], 0, s[44:45]
	s_mov_b32 s34, -8
	s_mov_b32 s35, 56
	s_lshl_b32 s45, s18, 1
	s_branch .LBB0_522

.LBB0_522:
	s_add_i32 s54, s34, 11
	s_add_i32 s55, s35, 4
	s_and_b64 s[18:19], s[4:5], exec
	s_cselect_b32 s18, s54, s55
	s_or_b32 s54, s18, s53
	s_lshl_b32 s18, s54, 4
	s_or_b32 s18, s18, s42
	s_ashr_i32 s19, s18, 31
	s_lshl_b64 s[18:19], s[18:19], 14
	s_or_b32 s18, s18, s45
	v_lshl_add_u64 v[60:61], v[92:93], 0, s[18:19]
	s_waitcnt lgkmcnt(1)
	v_lshl_add_u64 v[64:65], v[94:95], 0, s[18:19]
	global_load_dwordx4 v[56:59], v[60:61], off
	s_nop 0
	global_load_dwordx4 v[60:63], v[60:61], off offset:1024
	s_nop 0
	global_load_dwordx2 v[102:103], v[64:65], off
	ds_read_b128 v[64:67], v110
	s_waitcnt lgkmcnt(1)
	ds_read_b128 v[68:71], v110 offset:1024
	s_waitcnt vmcnt(21)
	v_lshlrev_b32_e32 v72, 16, v88
	v_and_b32_e32 v73, 0xffff0000, v88
	v_lshlrev_b32_e32 v74, 16, v89
	v_and_b32_e32 v75, 0xffff0000, v89
	s_mov_b64 s[18:19], -1
	s_and_b64 vcc, exec, s[16:17]
	s_cbranch_vccz .LBB0_524
	s_waitcnt lgkmcnt(1)
	v_mfma_f32_16x16x32_bf16 v[120:123], v[64:67], v[28:31], v[72:75]
	s_mov_b64 s[18:19], 0
	s_waitcnt lgkmcnt(0)
	v_mfma_f32_16x16x32_bf16 v[120:123], v[68:71], v[24:27], v[120:123]
	s_nop 7
	v_cvt_pk_bf16_f32 v88, v120, v121
	v_lshl_or_b32 v120, s52, 6, v104
	v_ashrrev_i32_e32 v121, 31, v120
	v_lshlrev_b64 v[120:121], 11, v[120:121]
	v_cvt_pk_bf16_f32 v89, v122, v123
	v_lshl_add_u64 v[120:121], v[90:91], 0, v[120:121]
	global_store_dwordx2 v[120:121], v[88:89], off

.LBB0_526:
	s_add_i32 s52, s34, 12
	s_add_i32 s55, s35, 3
	s_and_b64 s[18:19], s[4:5], exec
	s_cselect_b32 s18, s52, s55
	s_add_i32 s52, s18, s53
	s_lshl_b32 s18, s52, 4
	s_or_b32 s18, s18, s42
	s_ashr_i32 s19, s18, 31
	s_lshl_b64 s[18:19], s[18:19], 14
	s_or_b32 s18, s18, s45
	s_waitcnt lgkmcnt(0)
	s_barrier
	v_lshl_add_u64 v[24:25], v[92:93], 0, s[18:19]
	s_waitcnt lgkmcnt(1)
	v_lshl_add_u64 v[64:65], v[94:95], 0, s[18:19]
	global_load_dwordx4 v[28:31], v[24:25], off
	s_nop 0
	global_load_dwordx4 v[24:27], v[24:25], off offset:1024
	s_nop 0
	global_load_dwordx2 v[88:89], v[64:65], off
	ds_read_b128 v[64:67], v110 offset:2048
	s_waitcnt lgkmcnt(1)
	ds_read_b128 v[68:71], v110 offset:3072
	s_waitcnt vmcnt(21)
	v_lshlrev_b32_e32 v72, 16, v84
	v_and_b32_e32 v73, 0xffff0000, v84
	v_lshlrev_b32_e32 v74, 16, v85
	v_and_b32_e32 v75, 0xffff0000, v85
	s_mov_b64 s[18:19], -1
	s_and_b64 vcc, exec, s[16:17]
	s_cbranch_vccz .LBB0_528
	s_waitcnt lgkmcnt(1)
	v_mfma_f32_16x16x32_bf16 v[120:123], v[64:67], v[20:23], v[72:75]
	s_mov_b64 s[18:19], 0
	s_waitcnt lgkmcnt(0)
	v_mfma_f32_16x16x32_bf16 v[120:123], v[68:71], v[16:19], v[120:123]
	s_nop 7
	v_cvt_pk_bf16_f32 v84, v120, v121
	v_lshl_or_b32 v120, s36, 6, v104
	v_ashrrev_i32_e32 v121, 31, v120
	v_lshlrev_b64 v[120:121], 11, v[120:121]
	v_cvt_pk_bf16_f32 v85, v122, v123
	v_lshl_add_u64 v[120:121], v[90:91], 0, v[120:121]
	global_store_dwordx2 v[120:121], v[84:85], off

.LBB0_530:
	s_add_i32 s36, s34, 13
	s_add_i32 s55, s35, 2
	s_and_b64 s[18:19], s[4:5], exec
	s_cselect_b32 s18, s36, s55
	s_or_b32 s36, s18, s53
	s_lshl_b32 s18, s36, 4
	s_or_b32 s18, s18, s42
	s_ashr_i32 s19, s18, 31
	s_lshl_b64 s[18:19], s[18:19], 14
	s_or_b32 s18, s18, s45
	s_waitcnt lgkmcnt(0)
	s_barrier
	v_lshl_add_u64 v[16:17], v[92:93], 0, s[18:19]
	s_waitcnt lgkmcnt(1)
	v_lshl_add_u64 v[64:65], v[94:95], 0, s[18:19]
	global_load_dwordx4 v[20:23], v[16:17], off
	s_nop 0
	global_load_dwordx4 v[16:19], v[16:17], off offset:1024
	s_nop 0
	global_load_dwordx2 v[84:85], v[64:65], off
	ds_read_b128 v[64:67], v110
	s_waitcnt lgkmcnt(1)
	ds_read_b128 v[68:71], v110 offset:1024
	s_waitcnt vmcnt(21)
	v_lshlrev_b32_e32 v72, 16, v86
	v_and_b32_e32 v73, 0xffff0000, v86
	v_lshlrev_b32_e32 v74, 16, v87
	v_and_b32_e32 v75, 0xffff0000, v87
	s_mov_b64 s[18:19], -1
	s_and_b64 vcc, exec, s[16:17]
	s_cbranch_vccz .LBB0_532
	s_waitcnt lgkmcnt(1)
	v_mfma_f32_16x16x32_bf16 v[120:123], v[64:67], v[0:3], v[72:75]
	s_mov_b64 s[18:19], 0
	s_waitcnt lgkmcnt(0)
	v_mfma_f32_16x16x32_bf16 v[120:123], v[68:71], v[4:7], v[120:123]
	s_nop 7
	v_cvt_pk_bf16_f32 v86, v120, v121
	v_lshl_or_b32 v120, s24, 6, v104
	v_ashrrev_i32_e32 v121, 31, v120
	v_lshlrev_b64 v[120:121], 11, v[120:121]
	v_cvt_pk_bf16_f32 v87, v122, v123
	v_lshl_add_u64 v[120:121], v[90:91], 0, v[120:121]
	global_store_dwordx2 v[120:121], v[86:87], off

.LBB0_534:
	s_add_i32 s24, s34, 14
	s_add_i32 s55, s35, 1
	s_and_b64 s[18:19], s[4:5], exec
	s_cselect_b32 s18, s24, s55
	s_or_b32 s24, s18, s53
	s_lshl_b32 s18, s24, 4
	s_or_b32 s18, s18, s42
	s_ashr_i32 s19, s18, 31
	s_lshl_b64 s[18:19], s[18:19], 14
	s_or_b32 s18, s18, s45
	s_waitcnt lgkmcnt(0)
	s_barrier
	v_lshl_add_u64 v[4:5], v[92:93], 0, s[18:19]
	s_waitcnt lgkmcnt(1)
	v_lshl_add_u64 v[64:65], v[94:95], 0, s[18:19]
	global_load_dwordx4 v[0:3], v[4:5], off
	s_nop 0
	global_load_dwordx4 v[4:7], v[4:5], off offset:1024
	s_nop 0
	global_load_dwordx2 v[86:87], v[64:65], off
	ds_read_b128 v[64:67], v110 offset:2048
	s_waitcnt lgkmcnt(1)
	ds_read_b128 v[68:71], v110 offset:3072
	s_waitcnt vmcnt(21)
	v_lshlrev_b32_e32 v72, 16, v82
	v_and_b32_e32 v73, 0xffff0000, v82
	v_lshlrev_b32_e32 v74, 16, v83
	v_and_b32_e32 v75, 0xffff0000, v83
	s_mov_b64 s[18:19], -1
	s_and_b64 vcc, exec, s[16:17]
	s_cbranch_vccz .LBB0_536
	s_waitcnt lgkmcnt(1)
	v_mfma_f32_16x16x32_bf16 v[120:123], v[64:67], v[8:11], v[72:75]
	s_mov_b64 s[18:19], 0
	s_waitcnt lgkmcnt(0)
	v_mfma_f32_16x16x32_bf16 v[120:123], v[68:71], v[12:15], v[120:123]
	s_nop 7
	v_cvt_pk_bf16_f32 v82, v120, v121
	v_lshl_or_b32 v120, s26, 6, v104
	v_ashrrev_i32_e32 v121, 31, v120
	v_lshlrev_b64 v[120:121], 11, v[120:121]
	v_cvt_pk_bf16_f32 v83, v122, v123
	v_lshl_add_u64 v[120:121], v[90:91], 0, v[120:121]
	global_store_dwordx2 v[120:121], v[82:83], off

.LBB0_538:
	s_add_i32 s26, s34, 15
	s_and_b64 s[18:19], s[4:5], exec
	s_cselect_b32 s18, s26, s35
	s_or_b32 s26, s18, s53
	s_lshl_b32 s18, s26, 4
	s_or_b32 s18, s18, s42
	s_ashr_i32 s19, s18, 31
	s_lshl_b64 s[18:19], s[18:19], 14
	s_or_b32 s18, s18, s45
	s_waitcnt lgkmcnt(0)
	s_barrier
	v_lshl_add_u64 v[12:13], v[92:93], 0, s[18:19]
	s_waitcnt lgkmcnt(1)
	v_lshl_add_u64 v[64:65], v[94:95], 0, s[18:19]
	global_load_dwordx4 v[8:11], v[12:13], off
	s_nop 0
	global_load_dwordx4 v[12:15], v[12:13], off offset:1024
	s_nop 0
	global_load_dwordx2 v[82:83], v[64:65], off
	ds_read_b128 v[64:67], v110
	s_waitcnt lgkmcnt(1)
	ds_read_b128 v[68:71], v110 offset:1024
	s_waitcnt vmcnt(21)
	v_lshlrev_b32_e32 v72, 16, v96
	v_and_b32_e32 v73, 0xffff0000, v96
	v_lshlrev_b32_e32 v74, 16, v97
	v_and_b32_e32 v75, 0xffff0000, v97
	s_mov_b64 s[18:19], -1
	s_and_b64 vcc, exec, s[16:17]
	s_cbranch_vccz .LBB0_540
	s_waitcnt lgkmcnt(1)
	v_mfma_f32_16x16x32_bf16 v[120:123], v[64:67], v[32:35], v[72:75]
	s_mov_b64 s[18:19], 0
	s_waitcnt lgkmcnt(0)
	v_mfma_f32_16x16x32_bf16 v[120:123], v[68:71], v[36:39], v[120:123]
	s_nop 7
	v_cvt_pk_bf16_f32 v96, v120, v121
	v_lshl_or_b32 v120, s56, 6, v104
	v_ashrrev_i32_e32 v121, 31, v120
	v_lshlrev_b64 v[120:121], 11, v[120:121]
	v_cvt_pk_bf16_f32 v97, v122, v123
	v_lshl_add_u64 v[120:121], v[90:91], 0, v[120:121]
	global_store_dwordx2 v[120:121], v[96:97], off

.LBB0_542:
	s_add_i32 s34, s34, 8
	s_min_u32 s18, s34, 55
	s_add_i32 s55, s18, 8
	s_sub_i32 s56, 55, s18
	s_and_b64 s[18:19], s[4:5], exec
	s_cselect_b32 s18, s55, s56
	s_add_i32 s56, s18, s53
	s_lshl_b32 s18, s56, 4
	s_or_b32 s18, s18, s42
	s_ashr_i32 s19, s18, 31
	s_lshl_b64 s[18:19], s[18:19], 14
	s_or_b32 s18, s18, s45
	s_waitcnt lgkmcnt(0)
	s_barrier
	v_lshl_add_u64 v[36:37], v[92:93], 0, s[18:19]
	s_waitcnt lgkmcnt(1)
	v_lshl_add_u64 v[64:65], v[94:95], 0, s[18:19]
	global_load_dwordx4 v[32:35], v[36:37], off
	s_nop 0
	global_load_dwordx4 v[36:39], v[36:37], off offset:1024
	s_nop 0
	global_load_dwordx2 v[96:97], v[64:65], off
	ds_read_b128 v[64:67], v110 offset:2048
	s_waitcnt lgkmcnt(1)
	ds_read_b128 v[68:71], v110 offset:3072
	s_waitcnt vmcnt(21)
	v_lshlrev_b32_e32 v72, 16, v98
	v_and_b32_e32 v73, 0xffff0000, v98
	v_lshlrev_b32_e32 v74, 16, v99
	v_and_b32_e32 v75, 0xffff0000, v99
	s_mov_b64 s[18:19], -1
	s_and_b64 vcc, exec, s[16:17]
	s_cbranch_vccz .LBB0_544
	s_waitcnt lgkmcnt(1)
	v_mfma_f32_16x16x32_bf16 v[120:123], v[64:67], v[40:43], v[72:75]
	s_mov_b64 s[18:19], 0
	s_waitcnt lgkmcnt(0)
	v_mfma_f32_16x16x32_bf16 v[120:123], v[68:71], v[44:47], v[120:123]
	s_nop 7
	v_cvt_pk_bf16_f32 v98, v120, v121
	v_lshl_or_b32 v120, s57, 6, v104
	v_ashrrev_i32_e32 v121, 31, v120
	v_lshlrev_b64 v[120:121], 11, v[120:121]
	v_cvt_pk_bf16_f32 v99, v122, v123
	v_lshl_add_u64 v[120:121], v[90:91], 0, v[120:121]
	global_store_dwordx2 v[120:121], v[98:99], off

.LBB0_546:
	s_min_u32 s18, s34, 54
	s_add_i32 s55, s18, 9
	s_sub_i32 s57, 54, s18
	s_and_b64 s[18:19], s[4:5], exec
	s_cselect_b32 s18, s55, s57
	s_add_i32 s57, s18, s53
	s_lshl_b32 s18, s57, 4
	s_or_b32 s18, s18, s42
	s_ashr_i32 s19, s18, 31
	s_lshl_b64 s[18:19], s[18:19], 14
	s_or_b32 s18, s18, s45
	s_waitcnt lgkmcnt(0)
	s_barrier
	v_lshl_add_u64 v[44:45], v[92:93], 0, s[18:19]
	s_waitcnt lgkmcnt(1)
	v_lshl_add_u64 v[64:65], v[94:95], 0, s[18:19]
	global_load_dwordx4 v[40:43], v[44:45], off
	s_nop 0
	global_load_dwordx4 v[44:47], v[44:45], off offset:1024
	s_nop 0
	global_load_dwordx2 v[98:99], v[64:65], off
	ds_read_b128 v[64:67], v110
	s_waitcnt lgkmcnt(1)
	ds_read_b128 v[68:71], v110 offset:1024
	s_waitcnt vmcnt(21)
	v_lshlrev_b32_e32 v72, 16, v100
	v_and_b32_e32 v73, 0xffff0000, v100
	v_lshlrev_b32_e32 v74, 16, v101
	v_and_b32_e32 v75, 0xffff0000, v101
	s_mov_b64 s[18:19], -1
	s_and_b64 vcc, exec, s[16:17]
	s_cbranch_vccz .LBB0_548
	s_waitcnt lgkmcnt(1)
	v_mfma_f32_16x16x32_bf16 v[120:123], v[64:67], v[48:51], v[72:75]
	s_mov_b64 s[18:19], 0
	s_waitcnt lgkmcnt(0)
	v_mfma_f32_16x16x32_bf16 v[120:123], v[68:71], v[52:55], v[120:123]
	s_nop 7
	v_cvt_pk_bf16_f32 v100, v120, v121
	v_lshl_or_b32 v120, s60, 6, v104
	v_ashrrev_i32_e32 v121, 31, v120
	v_lshlrev_b64 v[120:121], 11, v[120:121]
	v_cvt_pk_bf16_f32 v101, v122, v123
	v_lshl_add_u64 v[120:121], v[90:91], 0, v[120:121]
	global_store_dwordx2 v[120:121], v[100:101], off

.LBB0_550:
	s_min_u32 s18, s34, 53
	s_add_i32 s55, s18, 10
	s_sub_i32 s60, 53, s18
	s_and_b64 s[18:19], s[4:5], exec
	s_cselect_b32 s18, s55, s60
	s_add_i32 s60, s18, s53
	s_lshl_b32 s18, s60, 4
	s_or_b32 s18, s18, s42
	s_ashr_i32 s19, s18, 31
	s_lshl_b64 s[18:19], s[18:19], 14
	s_or_b32 s18, s18, s45
	s_waitcnt lgkmcnt(0)
	s_barrier
	v_lshl_add_u64 v[52:53], v[92:93], 0, s[18:19]
	s_waitcnt lgkmcnt(1)
	v_lshl_add_u64 v[64:65], v[94:95], 0, s[18:19]
	global_load_dwordx4 v[48:51], v[52:53], off
	s_nop 0
	global_load_dwordx4 v[52:55], v[52:53], off offset:1024
	s_nop 0
	global_load_dwordx2 v[100:101], v[64:65], off
	ds_read_b128 v[64:67], v110 offset:2048
	s_waitcnt lgkmcnt(1)
	ds_read_b128 v[68:71], v110 offset:3072
	s_waitcnt vmcnt(21)
	v_lshlrev_b32_e32 v72, 16, v102
	v_and_b32_e32 v73, 0xffff0000, v102
	v_lshlrev_b32_e32 v74, 16, v103
	v_and_b32_e32 v75, 0xffff0000, v103
	s_mov_b64 s[18:19], -1
	s_and_b64 vcc, exec, s[16:17]
	s_cbranch_vccz .LBB0_552
	s_waitcnt lgkmcnt(1)
	v_mfma_f32_16x16x32_bf16 v[120:123], v[64:67], v[56:59], v[72:75]
	s_mov_b64 s[18:19], 0
	s_waitcnt lgkmcnt(0)
	v_mfma_f32_16x16x32_bf16 v[120:123], v[68:71], v[60:63], v[120:123]
	s_nop 7
	v_cvt_pk_bf16_f32 v102, v120, v121
	v_lshl_or_b32 v120, s54, 6, v104
	v_ashrrev_i32_e32 v121, 31, v120
	v_lshlrev_b64 v[120:121], 11, v[120:121]
	v_cvt_pk_bf16_f32 v103, v122, v123
	v_lshl_add_u64 v[120:121], v[90:91], 0, v[120:121]
	global_store_dwordx2 v[120:121], v[102:103], off
